# v66 variant: the arrival-time buffer_inv is issued by wave 1 after the entry rendezvous (own vmcnt), off wave 0's arrive/write-back/publish chain
# speedup vs baseline: 1.0010x; 1.0010x over previous
; __device__ __forceinline__ unsigned xb_add(unsigned* p, unsigned v) { return __hip_atomic_fetch_add(p, v, __ATOMIC_RELAXED, __HIP_MEMORY_SCOPE_AGENT); }
; __device__ __forceinline__ void xcd_barrier(const XcdBarrier& b) {
;     asm volatile("s_waitcnt vmcnt(0)" ::: "memory");
;     __syncthreads();
;     if (threadIdx.x == 0) {
;         unsigned* bar = b.bar;
;         __builtin_amdgcn_s_waitcnt(0);
;         unsigned nloc = b.st[0], nx = b.st[1];
;         if (nloc == 0u) { xcd_barrier_complete(bar, b.x, nloc, nx); b.st[0] = nloc; b.st[1] = nx; }
;         const unsigned old = xb_add(&bar[XB_XSUB(b.x)], 1u);
.LBB0_146:
	s_cmp_gt_i32 s35, 1
	s_cselect_b64 s[40:41], -1, 0
	s_and_b64 s[0:1], s[12:13], s[40:41]
	s_andn2_b64 vcc, exec, s[0:1]
	s_cbranch_vccnz .LBB0_192
	s_waitcnt vmcnt(0)
	v_cmp_eq_u32_e32 vcc, 0, v0
	s_waitcnt lgkmcnt(0)
	s_barrier
	s_cmp_lg_u32 s3, 1
	s_cbranch_scc1 .Lbinv_0
	buffer_inv sc1
.Lbinv_0:
	s_and_saveexec_b64 s[42:43], vcc
	s_cbranch_execz .LBB0_191
	v_mov_b32_e32 v2, s57
	s_waitcnt vmcnt(0) expcnt(0) lgkmcnt(0)
	ds_read_b32 v4, v2
	ds_read_b32 v2, v2 offset:4
	s_waitcnt lgkmcnt(1)
	v_cmp_ne_u32_e32 vcc, 0, v4
	s_cbranch_vccnz .LBB0_162
	s_add_u32 s0, s36, 0x4200
	s_addc_u32 s1, s37, 0
	s_add_u32 s6, s36, 0x4400
	s_addc_u32 s7, s37, 0
	s_add_u32 s8, s36, 0x4500
	s_addc_u32 s9, s37, 0
	s_add_u32 s10, s36, 0x4600
	s_addc_u32 s11, s37, 0
	s_add_u32 s12, s36, 0x4700
	s_addc_u32 s13, s37, 0
	s_add_u32 s14, s36, 0x4800
	s_addc_u32 s15, s37, 0
	s_add_u32 s16, s36, 0x4900
	s_addc_u32 s17, s37, 0
	s_add_u32 s18, s36, 0x4a00
	s_addc_u32 s19, s37, 0
	s_add_u32 s20, s36, 0x4b00
	s_addc_u32 s21, s37, 0
	s_add_u32 s24, s36, 0x4c00
	s_addc_u32 s25, s37, 0
	s_add_u32 s26, s36, 0x4d00
	s_addc_u32 s27, s37, 0
	s_add_u32 s28, s36, 0x4e00
	s_addc_u32 s29, s37, 0
	s_add_u32 s30, s36, 0x4f00
	s_addc_u32 s31, s37, 0
	s_add_u32 s44, s36, 0x5000
	s_addc_u32 s45, s37, 0
	s_load_dwordx2 s[4:5], s[38:39], 0x4
	s_add_u32 s46, s36, 0x5100
	s_addc_u32 s47, s37, 0
	s_add_u32 s48, s36, 0x5200
	s_addc_u32 s49, s37, 0
	s_add_u32 s50, s36, 0x5300
	s_waitcnt lgkmcnt(0)
	s_mul_i32 s22, s4, s33
	s_addc_u32 s51, s37, 0
	s_mul_i32 s22, s22, s5
	s_mov_b32 s23, 1
	s_mov_b64 s[4:5], 0
	v_mov_b64_e32 v[2:3], s[6:7]
	v_mov_b64_e32 v[4:5], s[8:9]
	v_mov_b64_e32 v[6:7], s[10:11]
	v_mov_b64_e32 v[8:9], s[12:13]
	v_mov_b64_e32 v[10:11], s[14:15]
	v_mov_b64_e32 v[12:13], s[16:17]
	v_mov_b64_e32 v[14:15], s[18:19]
	v_mov_b64_e32 v[16:17], s[20:21]
	v_mov_b64_e32 v[18:19], s[24:25]
	v_mov_b64_e32 v[20:21], s[26:27]
	v_mov_b64_e32 v[22:23], s[28:29]
	v_mov_b64_e32 v[24:25], s[30:31]
	v_mov_b64_e32 v[26:27], s[44:45]
	v_mov_b64_e32 v[28:29], s[46:47]
	v_mov_b64_e32 v[30:31], s[48:49]
	v_mov_b64_e32 v[32:33], s[50:51]
	s_branch .LBB0_152

; __device__ __forceinline__ void xcd_barrier(const XcdBarrier& b) {
;     ...
;     __syncthreads();
.LBB0_191:
	s_or_b64 exec, exec, s[42:43]
	s_waitcnt vmcnt(0) lgkmcnt(0)
	s_barrier

; __device__ __forceinline__ unsigned xb_add(unsigned* p, unsigned v) { return __hip_atomic_fetch_add(p, v, __ATOMIC_RELAXED, __HIP_MEMORY_SCOPE_AGENT); }
; __device__ __forceinline__ void xcd_barrier(const XcdBarrier& b) {
;     asm volatile("s_waitcnt vmcnt(0)" ::: "memory");
;     __syncthreads();
;     if (threadIdx.x == 0) {
;         unsigned* bar = b.bar;
;         __builtin_amdgcn_s_waitcnt(0);
;         unsigned nloc = b.st[0], nx = b.st[1];
;         if (nloc == 0u) { xcd_barrier_complete(bar, b.x, nloc, nx); b.st[0] = nloc; b.st[1] = nx; }
;         const unsigned old = xb_add(&bar[XB_XSUB(b.x)], 1u);
.LBB0_208:
	s_cmp_gt_i32 s35, 2
	s_cselect_b64 s[40:41], -1, 0
	s_and_b64 s[0:1], s[0:1], s[40:41]
	s_andn2_b64 vcc, exec, s[0:1]
	s_cbranch_vccnz .LBB0_254
	s_waitcnt vmcnt(0)
	v_cmp_eq_u32_e32 vcc, 0, v0
	s_waitcnt lgkmcnt(0)
	s_barrier
	s_cmp_lg_u32 s3, 1
	s_cbranch_scc1 .Lbinv_1
	buffer_inv sc1

; __device__ __forceinline__ unsigned xb_add(unsigned* p, unsigned v) { return __hip_atomic_fetch_add(p, v, __ATOMIC_RELAXED, __HIP_MEMORY_SCOPE_AGENT); }
; __device__ __forceinline__ void xcd_barrier(const XcdBarrier& b) {
;     asm volatile("s_waitcnt vmcnt(0)" ::: "memory");
;     __syncthreads();
;     if (threadIdx.x == 0) {
;         unsigned* bar = b.bar;
;         __builtin_amdgcn_s_waitcnt(0);
;         unsigned nloc = b.st[0], nx = b.st[1];
;         if (nloc == 0u) { xcd_barrier_complete(bar, b.x, nloc, nx); b.st[0] = nloc; b.st[1] = nx; }
;         const unsigned old = xb_add(&bar[XB_XSUB(b.x)], 1u);
.LBB0_308:
	s_cmp_gt_i32 s35, 3
	s_cselect_b64 s[40:41], -1, 0
	s_and_b64 s[0:1], s[4:5], s[40:41]
	s_andn2_b64 vcc, exec, s[0:1]
	s_cbranch_vccnz .LBB0_354
	s_waitcnt vmcnt(0)
	v_cmp_eq_u32_e32 vcc, 0, v0
	s_waitcnt lgkmcnt(0)
	s_barrier
	s_cmp_lg_u32 s3, 1
	s_cbranch_scc1 .Lbinv_2
	buffer_inv sc1

; __device__ __forceinline__ unsigned xb_add(unsigned* p, unsigned v) { return __hip_atomic_fetch_add(p, v, __ATOMIC_RELAXED, __HIP_MEMORY_SCOPE_AGENT); }
; __device__ __forceinline__ void xcd_barrier(const XcdBarrier& b) {
;     asm volatile("s_waitcnt vmcnt(0)" ::: "memory");
;     __syncthreads();
;     if (threadIdx.x == 0) {
;         unsigned* bar = b.bar;
;         __builtin_amdgcn_s_waitcnt(0);
;         unsigned nloc = b.st[0], nx = b.st[1];
;         if (nloc == 0u) { xcd_barrier_complete(bar, b.x, nloc, nx); b.st[0] = nloc; b.st[1] = nx; }
;         const unsigned old = xb_add(&bar[XB_XSUB(b.x)], 1u);
.LBB0_435:
	s_cmp_gt_i32 s35, 4
	s_cselect_b64 s[40:41], -1, 0
	s_and_b64 s[0:1], s[6:7], s[40:41]
	s_andn2_b64 vcc, exec, s[0:1]
	s_cbranch_vccnz .LBB0_481
	s_waitcnt vmcnt(0)
	v_cmp_eq_u32_e32 vcc, 0, v0
	s_waitcnt vmcnt(0) lgkmcnt(0)
	s_barrier
	s_cmp_lg_u32 s3, 1
	s_cbranch_scc1 .Lbinv_3
	buffer_inv sc1

; __device__ __forceinline__ unsigned xb_add(unsigned* p, unsigned v) { return __hip_atomic_fetch_add(p, v, __ATOMIC_RELAXED, __HIP_MEMORY_SCOPE_AGENT); }
; __device__ __forceinline__ void xcd_barrier(const XcdBarrier& b) {
;     asm volatile("s_waitcnt vmcnt(0)" ::: "memory");
;     __syncthreads();
;     if (threadIdx.x == 0) {
;         unsigned* bar = b.bar;
;         __builtin_amdgcn_s_waitcnt(0);
;         unsigned nloc = b.st[0], nx = b.st[1];
;         if (nloc == 0u) { xcd_barrier_complete(bar, b.x, nloc, nx); b.st[0] = nloc; b.st[1] = nx; }
;         const unsigned old = xb_add(&bar[XB_XSUB(b.x)], 1u);
.LBB0_521:
	s_cmp_gt_i32 s35, 5
	s_cselect_b64 s[40:41], -1, 0
	s_and_b64 s[0:1], s[4:5], s[40:41]
	s_andn2_b64 vcc, exec, s[0:1]
	s_cbranch_vccnz .LBB0_567
	s_waitcnt vmcnt(0)
	v_cmp_eq_u32_e32 vcc, 0, v0
	s_waitcnt vmcnt(0) lgkmcnt(0)
	s_barrier
	s_cmp_lg_u32 s3, 1
	s_cbranch_scc1 .Lbinv_4
	buffer_inv sc1

; __device__ __forceinline__ unsigned xb_add(unsigned* p, unsigned v) { return __hip_atomic_fetch_add(p, v, __ATOMIC_RELAXED, __HIP_MEMORY_SCOPE_AGENT); }
; __device__ __forceinline__ void xcd_barrier(const XcdBarrier& b) {
;     asm volatile("s_waitcnt vmcnt(0)" ::: "memory");
;     __syncthreads();
;     if (threadIdx.x == 0) {
;         unsigned* bar = b.bar;
;         __builtin_amdgcn_s_waitcnt(0);
;         unsigned nloc = b.st[0], nx = b.st[1];
;         if (nloc == 0u) { xcd_barrier_complete(bar, b.x, nloc, nx); b.st[0] = nloc; b.st[1] = nx; }
;         const unsigned old = xb_add(&bar[XB_XSUB(b.x)], 1u);
.LBB0_620:
	s_cmp_gt_i32 s35, 6
	s_cselect_b64 s[40:41], -1, 0
	s_and_b64 s[0:1], s[4:5], s[40:41]
	s_andn2_b64 vcc, exec, s[0:1]
	s_cbranch_vccnz .LBB0_666
	s_waitcnt vmcnt(0)
	v_cmp_eq_u32_e32 vcc, 0, v0
	s_waitcnt vmcnt(0) lgkmcnt(0)
	s_barrier
	s_cmp_lg_u32 s3, 1
	s_cbranch_scc1 .Lbinv_5
	buffer_inv sc1

; __device__ __forceinline__ unsigned xb_add(unsigned* p, unsigned v) { return __hip_atomic_fetch_add(p, v, __ATOMIC_RELAXED, __HIP_MEMORY_SCOPE_AGENT); }
; __device__ __forceinline__ void xcd_barrier(const XcdBarrier& b) {
;     asm volatile("s_waitcnt vmcnt(0)" ::: "memory");
;     __syncthreads();
;     if (threadIdx.x == 0) {
;         unsigned* bar = b.bar;
;         __builtin_amdgcn_s_waitcnt(0);
;         unsigned nloc = b.st[0], nx = b.st[1];
;         if (nloc == 0u) { xcd_barrier_complete(bar, b.x, nloc, nx); b.st[0] = nloc; b.st[1] = nx; }
;         const unsigned old = xb_add(&bar[XB_XSUB(b.x)], 1u);
.LBB0_699:
	s_cmp_gt_i32 s35, 7
	s_cselect_b64 s[40:41], -1, 0
	s_and_b64 s[0:1], s[0:1], s[40:41]
	s_andn2_b64 vcc, exec, s[0:1]
	s_cbranch_vccnz .LBB0_745
	s_waitcnt vmcnt(0)
	v_cmp_eq_u32_e32 vcc, 0, v0
	s_waitcnt vmcnt(0) lgkmcnt(0)
	s_barrier
	s_cmp_lg_u32 s3, 1
	s_cbranch_scc1 .Lbinv_6
	buffer_inv sc1

; __device__ __forceinline__ unsigned xb_add(unsigned* p, unsigned v) { return __hip_atomic_fetch_add(p, v, __ATOMIC_RELAXED, __HIP_MEMORY_SCOPE_AGENT); }
; __device__ __forceinline__ void xcd_barrier(const XcdBarrier& b) {
;     asm volatile("s_waitcnt vmcnt(0)" ::: "memory");
;     __syncthreads();
;     if (threadIdx.x == 0) {
;         unsigned* bar = b.bar;
;         __builtin_amdgcn_s_waitcnt(0);
;         unsigned nloc = b.st[0], nx = b.st[1];
;         if (nloc == 0u) { xcd_barrier_complete(bar, b.x, nloc, nx); b.st[0] = nloc; b.st[1] = nx; }
;         const unsigned old = xb_add(&bar[XB_XSUB(b.x)], 1u);
.LBB0_770:
	s_cmp_gt_i32 s35, 8
	s_cselect_b64 s[40:41], -1, 0
	s_and_b64 s[0:1], s[4:5], s[40:41]
	s_andn2_b64 vcc, exec, s[0:1]
	s_cbranch_vccnz .LBB0_816
	s_waitcnt vmcnt(0)
	v_cmp_eq_u32_e32 vcc, 0, v0
	s_waitcnt vmcnt(0) lgkmcnt(0)
	s_barrier
	s_cmp_lg_u32 s3, 1
	s_cbranch_scc1 .Lbinv_7
	buffer_inv sc1

; __device__ __forceinline__ unsigned xb_add(unsigned* p, unsigned v) { return __hip_atomic_fetch_add(p, v, __ATOMIC_RELAXED, __HIP_MEMORY_SCOPE_AGENT); }
; __device__ __forceinline__ void xcd_barrier(const XcdBarrier& b) {
;     asm volatile("s_waitcnt vmcnt(0)" ::: "memory");
;     __syncthreads();
;     if (threadIdx.x == 0) {
;         unsigned* bar = b.bar;
;         __builtin_amdgcn_s_waitcnt(0);
;         unsigned nloc = b.st[0], nx = b.st[1];
;         if (nloc == 0u) { xcd_barrier_complete(bar, b.x, nloc, nx); b.st[0] = nloc; b.st[1] = nx; }
;         const unsigned old = xb_add(&bar[XB_XSUB(b.x)], 1u);
.LBB0_847:
	s_cmp_gt_i32 s35, 9
	s_cselect_b64 s[40:41], -1, 0
	s_and_b64 s[0:1], s[4:5], s[40:41]
	s_andn2_b64 vcc, exec, s[0:1]
	s_cbranch_vccnz .LBB0_893
	s_waitcnt vmcnt(0)
	v_cmp_eq_u32_e32 vcc, 0, v0
	s_waitcnt vmcnt(0) lgkmcnt(0)
	s_barrier
	s_cmp_lg_u32 s3, 1
	s_cbranch_scc1 .Lbinv_8
	buffer_inv sc1

; __device__ __forceinline__ unsigned xb_add(unsigned* p, unsigned v) { return __hip_atomic_fetch_add(p, v, __ATOMIC_RELAXED, __HIP_MEMORY_SCOPE_AGENT); }
; __device__ __forceinline__ void xcd_barrier(const XcdBarrier& b) {
;     asm volatile("s_waitcnt vmcnt(0)" ::: "memory");
;     __syncthreads();
;     if (threadIdx.x == 0) {
;         unsigned* bar = b.bar;
;         __builtin_amdgcn_s_waitcnt(0);
;         unsigned nloc = b.st[0], nx = b.st[1];
;         if (nloc == 0u) { xcd_barrier_complete(bar, b.x, nloc, nx); b.st[0] = nloc; b.st[1] = nx; }
;         const unsigned old = xb_add(&bar[XB_XSUB(b.x)], 1u);
.LBB0_918:
	s_cmp_gt_i32 s35, 10
	s_cselect_b64 s[40:41], -1, 0
	s_and_b64 s[0:1], s[4:5], s[40:41]
	s_andn2_b64 vcc, exec, s[0:1]
	s_cbranch_vccnz .LBB0_964
	s_waitcnt vmcnt(0)
	v_cmp_eq_u32_e32 vcc, 0, v0
	s_waitcnt vmcnt(0) lgkmcnt(0)
	s_barrier
	s_cmp_lg_u32 s3, 1
	s_cbranch_scc1 .Lbinv_9
	buffer_inv sc1

; __device__ __forceinline__ unsigned xb_add(unsigned* p, unsigned v) { return __hip_atomic_fetch_add(p, v, __ATOMIC_RELAXED, __HIP_MEMORY_SCOPE_AGENT); }
; __device__ __forceinline__ void xcd_barrier(const XcdBarrier& b) {
;     asm volatile("s_waitcnt vmcnt(0)" ::: "memory");
;     __syncthreads();
;     if (threadIdx.x == 0) {
;         unsigned* bar = b.bar;
;         __builtin_amdgcn_s_waitcnt(0);
;         unsigned nloc = b.st[0], nx = b.st[1];
;         if (nloc == 0u) { xcd_barrier_complete(bar, b.x, nloc, nx); b.st[0] = nloc; b.st[1] = nx; }
;         const unsigned old = xb_add(&bar[XB_XSUB(b.x)], 1u);
.LBB0_987:
	s_cmp_gt_i32 s35, 11
	s_cselect_b64 s[40:41], -1, 0
	s_and_b64 s[0:1], s[26:27], s[40:41]
	s_andn2_b64 vcc, exec, s[0:1]
	s_cbranch_vccnz .LBB0_1033
	s_waitcnt vmcnt(0)
	v_cmp_eq_u32_e32 vcc, 0, v0
	s_waitcnt vmcnt(0) lgkmcnt(0)
	s_barrier
	s_cmp_lg_u32 s3, 1
	s_cbranch_scc1 .Lbinv_10
	buffer_inv sc1

; __device__ __forceinline__ unsigned xb_add(unsigned* p, unsigned v) { return __hip_atomic_fetch_add(p, v, __ATOMIC_RELAXED, __HIP_MEMORY_SCOPE_AGENT); }
; __device__ __forceinline__ void xcd_barrier(const XcdBarrier& b) {
;     asm volatile("s_waitcnt vmcnt(0)" ::: "memory");
;     __syncthreads();
;     if (threadIdx.x == 0) {
;         unsigned* bar = b.bar;
;         __builtin_amdgcn_s_waitcnt(0);
;         unsigned nloc = b.st[0], nx = b.st[1];
;         if (nloc == 0u) { xcd_barrier_complete(bar, b.x, nloc, nx); b.st[0] = nloc; b.st[1] = nx; }
;         const unsigned old = xb_add(&bar[XB_XSUB(b.x)], 1u);
.LBB0_1076:
	s_cmp_gt_i32 s35, 12
	s_cselect_b64 s[40:41], -1, 0
	s_and_b64 s[0:1], s[4:5], s[40:41]
	s_andn2_b64 vcc, exec, s[0:1]
	s_cbranch_vccnz .LBB0_1122
	s_waitcnt vmcnt(0)
	v_cmp_eq_u32_e32 vcc, 0, v0
	s_waitcnt vmcnt(0) lgkmcnt(0)
	s_barrier
	s_cmp_lg_u32 s3, 1
	s_cbranch_scc1 .Lbinv_11
	buffer_inv sc1

; __device__ __forceinline__ unsigned xb_add(unsigned* p, unsigned v) { return __hip_atomic_fetch_add(p, v, __ATOMIC_RELAXED, __HIP_MEMORY_SCOPE_AGENT); }
; __device__ __forceinline__ void xcd_barrier(const XcdBarrier& b) {
;     asm volatile("s_waitcnt vmcnt(0)" ::: "memory");
;     __syncthreads();
;     if (threadIdx.x == 0) {
;         unsigned* bar = b.bar;
;         __builtin_amdgcn_s_waitcnt(0);
;         unsigned nloc = b.st[0], nx = b.st[1];
;         if (nloc == 0u) { xcd_barrier_complete(bar, b.x, nloc, nx); b.st[0] = nloc; b.st[1] = nx; }
;         const unsigned old = xb_add(&bar[XB_XSUB(b.x)], 1u);
.LBB0_1161:
	s_cmp_gt_i32 s35, 13
	s_cselect_b64 s[40:41], -1, 0
	s_and_b64 s[0:1], s[0:1], s[40:41]
	s_andn2_b64 vcc, exec, s[0:1]
	s_cbranch_vccnz .LBB0_1207
	s_waitcnt vmcnt(0)
	v_cmp_eq_u32_e32 vcc, 0, v0
	s_waitcnt vmcnt(0) lgkmcnt(0)
	s_barrier
	s_cmp_lg_u32 s3, 1
	s_cbranch_scc1 .Lbinv_12
	buffer_inv sc1
.Lbinv_12:
	s_and_saveexec_b64 s[42:43], vcc
	s_cbranch_execz .LBB0_1206
	v_mov_b32_e32 v2, s57
	s_waitcnt vmcnt(0) expcnt(0) lgkmcnt(0)
	ds_read_b32 v4, v2
	ds_read_b32 v2, v2 offset:4
	s_waitcnt lgkmcnt(1)
	v_cmp_ne_u32_e32 vcc, 0, v4
	s_cbranch_vccnz .LBB0_1177
	s_add_u32 s0, s36, 0x4200
	s_addc_u32 s1, s37, 0
	s_add_u32 s6, s36, 0x4400
	s_addc_u32 s7, s37, 0
	s_add_u32 s8, s36, 0x4500
	s_addc_u32 s9, s37, 0
	s_add_u32 s10, s36, 0x4600
	s_addc_u32 s11, s37, 0
	s_add_u32 s12, s36, 0x4700
	s_addc_u32 s13, s37, 0
	s_add_u32 s14, s36, 0x4800
	s_addc_u32 s15, s37, 0
	s_add_u32 s16, s36, 0x4900
	s_addc_u32 s17, s37, 0
	s_add_u32 s18, s36, 0x4a00
	s_addc_u32 s19, s37, 0
	s_add_u32 s20, s36, 0x4b00
	s_addc_u32 s21, s37, 0
	s_add_u32 s24, s36, 0x4c00
	s_addc_u32 s25, s37, 0
	s_add_u32 s26, s36, 0x4d00
	s_addc_u32 s27, s37, 0
	s_add_u32 s28, s36, 0x4e00
	s_addc_u32 s29, s37, 0
	s_add_u32 s30, s36, 0x4f00
	s_addc_u32 s31, s37, 0
	s_load_dwordx2 s[4:5], s[38:39], 0x4
	s_add_u32 s38, s36, 0x5000
	s_addc_u32 s39, s37, 0
	s_add_u32 s44, s36, 0x5100
	s_addc_u32 s45, s37, 0
	s_add_u32 s46, s36, 0x5200
	s_addc_u32 s47, s37, 0
	s_add_u32 s48, s36, 0x5300
	s_waitcnt lgkmcnt(0)
	s_mul_i32 s22, s4, s33
	s_addc_u32 s49, s37, 0
	s_mul_i32 s22, s22, s5
	s_mov_b32 s23, 1
	s_mov_b64 s[4:5], 0
	v_mov_b64_e32 v[2:3], s[6:7]
	v_mov_b64_e32 v[4:5], s[8:9]
	v_mov_b64_e32 v[6:7], s[10:11]
	v_mov_b64_e32 v[8:9], s[12:13]
	v_mov_b64_e32 v[10:11], s[14:15]
	v_mov_b64_e32 v[12:13], s[16:17]
	v_mov_b64_e32 v[14:15], s[18:19]
	v_mov_b64_e32 v[16:17], s[20:21]
	v_mov_b64_e32 v[18:19], s[24:25]
	v_mov_b64_e32 v[20:21], s[26:27]
	v_mov_b64_e32 v[22:23], s[28:29]
	v_mov_b64_e32 v[24:25], s[30:31]
	v_mov_b64_e32 v[26:27], s[38:39]
	v_mov_b64_e32 v[28:29], s[44:45]
	v_mov_b64_e32 v[30:31], s[46:47]
	v_mov_b64_e32 v[32:33], s[48:49]
	s_branch .LBB0_1167
